# P9 epilogue f32 x residual loads tagged nt
# speedup vs baseline: 1.0274x; 1.0011x over previous
; __device__ __forceinline__ float sigmoidf_(float x) { return __builtin_amdgcn_rcpf(1.f + __builtin_amdgcn_exp2f(-1.4426950408889634f * x)); }
;     __device__ __forceinline__ void operator()(const f32x4 (&acc)[2][2][4][2], const Unit& u, int wr, int wc, int fr, int fq) const {
;     ...
;         EPB_LOAD(0);
; #pragma unroll
;         for (int kb = 0; kb < 8; ++kb) { const int ai = kb >> 2, m = kb & 3;
;             if (kb < 7) EPB_LOAD(kb + 1);
;             { const int row = row0 + ai * HALF + m * 16; float rmx = 0.f;
; #pragma unroll
;                 for (int bj = 0; bj < 2; ++bj) { const int col = col0 + bj * HALF; f32x4 v0 = acc[ai][bj][m][0], v1 = acc[ai][bj][m][1];
;                     if (QI8) { const f32x4 c0 = cb[bj][0] * ra[ai][m], c1 = cb[bj][1] * ra[ai][m]; const i32x4 i0 = __builtin_bit_cast(i32x4, v0), i1 = __builtin_bit_cast(i32x4, v1);
;                         v0 = (f32x4){(float)i0[0], (float)i0[1], (float)i0[2], (float)i0[3]} * c0; v1 = (f32x4){(float)i1[0], (float)i1[1], (float)i1[2], (float)i1[3]} * c1; }
;                     else if (MODE == 0) { v0 = v0 * tsc; v1 = v1 * tsc; }
;                     if (!QI8 && MODE == 1) { v0 = v0 * cb[bj][0]; v1 = v1 * cb[bj][1]; }
;                     if (MODE == 2 || MODE == 3) { const u32x4 g = gq[kb & 1][bj];
;                         f32x4 g0 = {sigmoidf_(bflo(g.x)), sigmoidf_(bfhi(g.x)), sigmoidf_(bflo(g.y)), sigmoidf_(bfhi(g.y))};
;                         f32x4 g1 = {sigmoidf_(bflo(g.z)), sigmoidf_(bfhi(g.z)), sigmoidf_(bflo(g.w)), sigmoidf_(bfhi(g.w))};
;                         v0 = v0 * g0; v1 = v1 * g1;
;                         if (MODE == 3) { const u32x4 q = aq[kb & 1][bj];
;                             v0 = v0 + (f32x4){bflo(q.x), bfhi(q.x), bflo(q.y), bfhi(q.y)}; v1 = v1 + (f32x4){bflo(q.z), bfhi(q.z), bflo(q.w), bfhi(q.w)}; } }
;                     if (MODE == 4) { v0 = v0 + rs[kb & 1][bj][0]; v1 = v1 + rs[kb & 1][bj][1]; }
.LBB0_1188:
	v_lshl_add_u32 v146, s26, 8, v1
	v_ashrrev_i32_e32 v147, 31, v146
	v_lshl_or_b32 v182, s58, 8, v224
	v_lshl_add_u64 v[178:179], v[146:147], 2, s[4:5]
	v_ashrrev_i32_e32 v183, 31, v182
	global_load_dword v180, v[178:179], off
	v_lshlrev_b64 v[148:149], 2, v[182:183]
	v_lshlrev_b64 v[150:151], 14, v[146:147]
	v_or_b32_e32 v186, 16, v146
	v_lshl_add_u64 v[110:111], s[8:9], 0, v[148:149]
	v_lshl_add_u64 v[150:151], s[0:1], 0, v[150:151]
	v_ashrrev_i32_e32 v187, 31, v186
	global_load_dwordx4 v[126:129], v[110:111], off nt
	global_load_dwordx4 v[122:125], v[110:111], off offset:16 nt
	global_load_dwordx4 v[106:109], v[110:111], off offset:528 nt
	s_nop 0
	global_load_dwordx4 v[110:113], v[110:111], off offset:512 nt
	v_lshl_add_u64 v[162:163], v[150:151], 0, v[148:149]
	v_lshlrev_b64 v[166:167], 14, v[186:187]
	global_load_dwordx4 v[150:153], v[162:163], off nt
	global_load_dwordx4 v[154:157], v[162:163], off offset:16 nt
	global_load_dwordx4 v[158:161], v[162:163], off offset:512 nt
	s_nop 0
	global_load_dwordx4 v[162:165], v[162:163], off offset:528 nt
	s_nop 0
	global_load_dword v184, v[178:179], off offset:64
	v_lshl_add_u64 v[166:167], s[0:1], 0, v[166:167]
	v_lshl_add_u64 v[174:175], v[166:167], 0, v[148:149]
	global_load_dwordx4 v[166:169], v[174:175], off nt
	global_load_dwordx4 v[170:173], v[174:175], off offset:16 nt
	v_cvt_f32_i32_e32 v189, v143
	v_cvt_f32_i32_e32 v188, v142
	v_cvt_f32_i32_e32 v191, v145
	v_cvt_f32_i32_e32 v190, v144
	global_load_dwordx4 v[142:145], v[174:175], off offset:528 nt
	s_nop 0
	global_load_dwordx4 v[174:177], v[174:175], off offset:512 nt
	v_cvt_f32_i32_e32 v193, v139
	v_cvt_f32_i32_e32 v192, v138
	v_cvt_f32_i32_e32 v213, v141
	v_cvt_f32_i32_e32 v212, v140
	v_cvt_f32_i32_e32 v215, v135
	v_cvt_f32_i32_e32 v214, v134
	v_cvt_f32_i32_e32 v217, v137
	v_cvt_f32_i32_e32 v216, v136
	v_cvt_f32_i32_e32 v219, v131
	v_cvt_f32_i32_e32 v218, v130
	v_cvt_f32_i32_e32 v221, v133
	v_cvt_f32_i32_e32 v220, v132
	v_or_b32_e32 v222, 32, v146
	v_lshlrev_b64 v[228:229], 13, v[146:147]
	v_cvt_f32_i32_e32 v119, v119
	v_cvt_f32_i32_e32 v118, v118
	v_lshlrev_b64 v[130:131], 1, v[182:183]
	v_ashrrev_i32_e32 v223, 31, v222
	global_load_dword v182, v[178:179], off offset:128
	global_load_dword v140, v[178:179], off offset:192
	global_load_dword v138, v[178:179], off offset:512
	global_load_dword v136, v[178:179], off offset:576
	global_load_dword v134, v[178:179], off offset:640
	global_load_dword v132, v[178:179], off offset:704
	v_lshl_add_u64 v[178:179], s[10:11], 0, v[228:229]
	v_cvt_f32_i32_e32 v115, v115
	v_cvt_f32_i32_e32 v117, v117
	v_cvt_f32_i32_e32 v116, v116
	v_cvt_f32_i32_e32 v114, v114
	v_lshlrev_b64 v[228:229], 14, v[222:223]
	v_lshl_add_u64 v[178:179], v[178:179], 0, v[130:131]
	v_lshl_add_u64 v[228:229], s[0:1], 0, v[228:229]
	v_cvt_f32_i32_e32 v121, v121
	v_cvt_f32_i32_e32 v120, v120
	v_lshl_add_u64 v[228:229], v[228:229], 0, v[148:149]
	v_cvt_f32_i32_e32 v103, v103
	v_cvt_f32_i32_e32 v102, v102
	v_cvt_f32_i32_e32 v101, v101
	v_cvt_f32_i32_e32 v100, v100
	v_cvt_f32_i32_e32 v105, v105
	v_cvt_f32_i32_e32 v104, v104
	v_cvt_f32_i32_e32 v99, v99
	v_cvt_f32_i32_e32 v98, v98
	v_cvt_f32_i32_e32 v97, v97
	v_cvt_f32_i32_e32 v96, v96
	v_cvt_f32_i32_e32 v87, v87
	v_cvt_f32_i32_e32 v86, v86
	v_cvt_f32_i32_e32 v89, v89
	v_cvt_f32_i32_e32 v88, v88
	v_cvt_f32_i32_e32 v83, v83
	v_cvt_f32_i32_e32 v85, v85
	v_cvt_f32_i32_e32 v84, v84
	v_cvt_f32_i32_e32 v82, v82
	v_cvt_f32_i32_e32 v79, v79
	v_cvt_f32_i32_e32 v78, v78
	v_cvt_f32_i32_e32 v75, v75
	v_cvt_f32_i32_e32 v77, v77
	v_cvt_f32_i32_e32 v76, v76
	v_cvt_f32_i32_e32 v74, v74
	v_cvt_f32_i32_e32 v81, v81
	v_cvt_f32_i32_e32 v80, v80
	v_cvt_f32_i32_e32 v71, v71
	v_cvt_f32_i32_e32 v70, v70
	v_cvt_f32_i32_e32 v67, v67
	v_cvt_f32_i32_e32 v69, v69
	v_cvt_f32_i32_e32 v68, v68
	v_cvt_f32_i32_e32 v66, v66
	v_cvt_f32_i32_e32 v73, v73
	v_cvt_f32_i32_e32 v72, v72
	v_cvt_f32_i32_e32 v63, v63
	s_waitcnt vmcnt(0)
	v_pk_mul_f32 v[230:231], v[180:181], v[126:127] op_sel_hi:[0,1]
	v_pk_mul_f32 v[232:233], v[180:181], v[128:129] op_sel_hi:[0,1]
	v_pk_mul_f32 v[234:235], v[180:181], v[122:123] op_sel_hi:[0,1]
	v_pk_mul_f32 v[236:237], v[180:181], v[124:125] op_sel_hi:[0,1]
	v_pk_fma_f32 v[152:153], v[232:233], v[190:191], v[152:153]
	v_pk_fma_f32 v[150:151], v[230:231], v[188:189], v[150:151]
	v_pk_mul_f32 v[238:239], v[180:181], v[110:111] op_sel_hi:[0,1]
	v_pk_mul_f32 v[240:241], v[180:181], v[112:113] op_sel_hi:[0,1]
	v_pk_mul_f32 v[242:243], v[180:181], v[106:107] op_sel_hi:[0,1]
	v_pk_mul_f32 v[180:181], v[180:181], v[108:109] op_sel_hi:[0,1]
	v_pk_fma_f32 v[156:157], v[236:237], v[212:213], v[156:157]
	v_pk_fma_f32 v[154:155], v[234:235], v[192:193], v[154:155]
	v_cvt_pk_bf16_f32 v150, v150, v151
	v_cvt_pk_bf16_f32 v151, v152, v153
	v_pk_fma_f32 v[160:161], v[240:241], v[216:217], v[160:161]
	v_cvt_pk_bf16_f32 v152, v154, v155
	v_cvt_pk_bf16_f32 v153, v156, v157
	v_pk_fma_f32 v[158:159], v[238:239], v[214:215], v[158:159]
	v_pk_fma_f32 v[164:165], v[180:181], v[220:221], v[164:165]
	v_pk_fma_f32 v[162:163], v[242:243], v[218:219], v[162:163]
	global_store_dwordx4 v[178:179], v[150:153], off
	v_pk_mul_f32 v[188:189], v[184:185], v[122:123] op_sel_hi:[0,1]
	v_pk_mul_f32 v[190:191], v[184:185], v[124:125] op_sel_hi:[0,1]
	v_cvt_pk_bf16_f32 v150, v158, v159
	v_cvt_pk_bf16_f32 v151, v160, v161
	v_cvt_pk_bf16_f32 v152, v162, v163
	v_cvt_pk_bf16_f32 v153, v164, v165
	global_store_dwordx4 v[178:179], v[150:153], off offset:256
	v_pk_mul_f32 v[178:179], v[184:185], v[126:127] op_sel_hi:[0,1]
	v_pk_fma_f32 v[118:119], v[178:179], v[118:119], v[166:167]
	global_load_dwordx4 v[150:153], v[228:229], off offset:16 nt
;     __device__ __forceinline__ void operator()(const f32x4 (&acc)[2][2][4][2], const Unit& u, int wr, int wc, int fr, int fq) const {
;     ...
;         EPB_LOAD(0);
; #pragma unroll
;         for (int kb = 0; kb < 8; ++kb) { const int ai = kb >> 2, m = kb & 3;
;             if (kb < 7) EPB_LOAD(kb + 1);
;             { const int row = row0 + ai * HALF + m * 16; float rmx = 0.f;
; #pragma unroll
;                 for (int bj = 0; bj < 2; ++bj) { const int col = col0 + bj * HALF; f32x4 v0 = acc[ai][bj][m][0], v1 = acc[ai][bj][m][1];
;                     if (QI8) { const f32x4 c0 = cb[bj][0] * ra[ai][m], c1 = cb[bj][1] * ra[ai][m]; const i32x4 i0 = __builtin_bit_cast(i32x4, v0), i1 = __builtin_bit_cast(i32x4, v1);
;                         v0 = (f32x4){(float)i0[0], (float)i0[1], (float)i0[2], (float)i0[3]} * c0; v1 = (f32x4){(float)i1[0], (float)i1[1], (float)i1[2], (float)i1[3]} * c1; }
;                     else if (MODE == 0) { v0 = v0 * tsc; v1 = v1 * tsc; }
;                     if (!QI8 && MODE == 1) { v0 = v0 * cb[bj][0]; v1 = v1 * cb[bj][1]; }
;                     if (MODE == 2 || MODE == 3) { const u32x4 g = gq[kb & 1][bj];
;                         f32x4 g0 = {sigmoidf_(bflo(g.x)), sigmoidf_(bfhi(g.x)), sigmoidf_(bflo(g.y)), sigmoidf_(bfhi(g.y))};
;                         f32x4 g1 = {sigmoidf_(bflo(g.z)), sigmoidf_(bfhi(g.z)), sigmoidf_(bflo(g.w)), sigmoidf_(bfhi(g.w))};
;                         v0 = v0 * g0; v1 = v1 * g1;
;                         if (MODE == 3) { const u32x4 q = aq[kb & 1][bj];
;                             v0 = v0 + (f32x4){bflo(q.x), bfhi(q.x), bflo(q.y), bfhi(q.y)}; v1 = v1 + (f32x4){bflo(q.z), bfhi(q.z), bflo(q.w), bfhi(q.w)}; } }
;                     if (MODE == 4) { v0 = v0 + rs[kb & 1][bj][0]; v1 = v1 + rs[kb & 1][bj][1]; }
;                     if (MODE == 5) { const u32x4 c = gq[kb & 1][bj], q = aq[kb & 1][bj];
;                         v0 = (f32x4){bflo(c.x) + sigmoidf_(v0[0]) * bflo(q.x), bfhi(c.x) + sigmoidf_(v0[1]) * bfhi(q.x), bflo(c.y) + sigmoidf_(v0[2]) * bflo(q.y), bfhi(c.y) + sigmoidf_(v0[3]) * bfhi(q.y)};
;                         v1 = (f32x4){bflo(c.z) + sigmoidf_(v1[0]) * bflo(q.z), bfhi(c.z) + sigmoidf_(v1[1]) * bfhi(q.z), bflo(c.w) + sigmoidf_(v1[2]) * bflo(q.w), bfhi(c.w) + sigmoidf_(v1[3]) * bfhi(q.w)}; }
	global_load_dwordx4 v[154:157], v[228:229], off nt
	global_load_dwordx4 v[158:161], v[228:229], off offset:528 nt
	global_load_dwordx4 v[162:165], v[228:229], off offset:512 nt
	v_pk_fma_f32 v[166:167], v[190:191], v[116:117], v[172:173]
	v_pk_fma_f32 v[116:117], v[188:189], v[114:115], v[170:171]
	v_cvt_pk_bf16_f32 v114, v118, v119
	v_lshlrev_b64 v[118:119], 13, v[186:187]
	v_pk_mul_f32 v[180:181], v[184:185], v[128:129] op_sel_hi:[0,1]
	v_lshl_add_u64 v[118:119], s[10:11], 0, v[118:119]
	v_pk_fma_f32 v[120:121], v[180:181], v[120:121], v[168:169]
	v_lshl_add_u64 v[118:119], v[118:119], 0, v[130:131]
	v_cvt_pk_bf16_f32 v115, v120, v121
	v_cvt_pk_bf16_f32 v116, v116, v117
	v_cvt_pk_bf16_f32 v117, v166, v167
	global_store_dwordx4 v[118:119], v[114:117], off
	v_pk_mul_f32 v[166:167], v[184:185], v[108:109] op_sel_hi:[0,1]
	v_pk_mul_f32 v[120:121], v[184:185], v[106:107] op_sel_hi:[0,1]
	v_pk_mul_f32 v[114:115], v[184:185], v[110:111] op_sel_hi:[0,1]
	v_pk_mul_f32 v[116:117], v[184:185], v[112:113] op_sel_hi:[0,1]
	v_pk_fma_f32 v[102:103], v[114:115], v[102:103], v[174:175]
	v_pk_fma_f32 v[114:115], v[166:167], v[100:101], v[144:145]
	v_or_b32_e32 v166, 48, v146
	v_pk_fma_f32 v[104:105], v[116:117], v[104:105], v[176:177]
	v_pk_fma_f32 v[100:101], v[120:121], v[98:99], v[142:143]
	v_cvt_pk_bf16_f32 v98, v102, v103
	v_cvt_pk_bf16_f32 v99, v104, v105
	v_ashrrev_i32_e32 v167, 31, v166
	v_cvt_pk_bf16_f32 v100, v100, v101
	v_cvt_pk_bf16_f32 v101, v114, v115
	global_store_dwordx4 v[118:119], v[98:101], off offset:256
	v_cvt_f32_i32_e32 v119, v95
	v_cvt_f32_i32_e32 v118, v94
	v_lshlrev_b64 v[98:99], 14, v[166:167]
	v_lshl_add_u64 v[98:99], s[0:1], 0, v[98:99]
	v_lshl_add_u64 v[114:115], v[98:99], 0, v[148:149]
	global_load_dwordx4 v[98:101], v[114:115], off nt
	global_load_dwordx4 v[102:105], v[114:115], off offset:16 nt
	v_cvt_f32_i32_e32 v143, v93
	v_cvt_f32_i32_e32 v142, v92
	global_load_dwordx4 v[92:95], v[114:115], off offset:528 nt
	s_nop 0
	global_load_dwordx4 v[114:117], v[114:115], off offset:512 nt
	v_cvt_f32_i32_e32 v121, v91
	v_cvt_f32_i32_e32 v120, v90
	v_lshlrev_b64 v[144:145], 13, v[222:223]
	v_pk_mul_f32 v[168:169], v[182:183], v[126:127] op_sel_hi:[0,1]
	v_lshl_add_u64 v[144:145], s[10:11], 0, v[144:145]
	v_pk_mul_f32 v[170:171], v[182:183], v[128:129] op_sel_hi:[0,1]
	v_pk_mul_f32 v[172:173], v[182:183], v[122:123] op_sel_hi:[0,1]
	v_lshl_add_u64 v[144:145], v[144:145], 0, v[130:131]
	v_pk_mul_f32 v[174:175], v[182:183], v[124:125] op_sel_hi:[0,1]
	v_add_u32_e32 v90, 0x80, v146
	v_pk_mul_f32 v[176:177], v[182:183], v[110:111] op_sel_hi:[0,1]
	v_pk_mul_f32 v[178:179], v[182:183], v[112:113] op_sel_hi:[0,1]
	v_ashrrev_i32_e32 v91, 31, v90
	v_cvt_f32_i32_e32 v62, v62
	v_cvt_f32_i32_e32 v59, v59
	v_cvt_f32_i32_e32 v61, v61
	v_cvt_f32_i32_e32 v60, v60
	v_cvt_f32_i32_e32 v58, v58
	v_cvt_f32_i32_e32 v65, v65
	v_cvt_f32_i32_e32 v64, v64
	v_cvt_f32_i32_e32 v55, v55
	v_cvt_f32_i32_e32 v54, v54
	v_cvt_f32_i32_e32 v53, v53
	v_cvt_f32_i32_e32 v52, v52
	v_cvt_f32_i32_e32 v57, v57
	v_cvt_f32_i32_e32 v56, v56
	v_cvt_f32_i32_e32 v51, v51
	v_cvt_f32_i32_e32 v50, v50
	v_cvt_f32_i32_e32 v47, v47
	v_cvt_f32_i32_e32 v46, v46
	v_cvt_f32_i32_e32 v43, v43
	v_cvt_f32_i32_e32 v45, v45
	v_cvt_f32_i32_e32 v44, v44
	v_cvt_f32_i32_e32 v42, v42
	v_cvt_f32_i32_e32 v49, v49
	v_cvt_f32_i32_e32 v48, v48
	v_cvt_f32_i32_e32 v39, v39
	v_cvt_f32_i32_e32 v38, v38
	v_cvt_f32_i32_e32 v37, v37
	v_cvt_f32_i32_e32 v36, v36
	s_waitcnt vmcnt(9)
	v_pk_fma_f32 v[120:121], v[172:173], v[120:121], v[150:151]
	s_waitcnt vmcnt(8)
	v_pk_fma_f32 v[118:119], v[168:169], v[118:119], v[154:155]
	v_pk_fma_f32 v[96:97], v[170:171], v[96:97], v[156:157]
	v_cvt_pk_bf16_f32 v118, v118, v119
	v_pk_fma_f32 v[142:143], v[174:175], v[142:143], v[152:153]
	v_cvt_pk_bf16_f32 v119, v96, v97
	v_cvt_pk_bf16_f32 v120, v120, v121
	v_pk_mul_f32 v[96:97], v[182:183], v[106:107] op_sel_hi:[0,1]
	v_cvt_pk_bf16_f32 v121, v142, v143
	global_store_dwordx4 v[144:145], v[118:121], off
	s_waitcnt vmcnt(7)
	v_pk_fma_f32 v[88:89], v[178:179], v[88:89], v[164:165]
	v_pk_fma_f32 v[86:87], v[176:177], v[86:87], v[162:163]
	v_pk_mul_f32 v[118:119], v[182:183], v[108:109] op_sel_hi:[0,1]
	v_pk_fma_f32 v[118:119], v[118:119], v[84:85], v[160:161]
	v_pk_fma_f32 v[84:85], v[96:97], v[82:83], v[158:159]
	v_cvt_pk_bf16_f32 v82, v86, v87
	v_cvt_pk_bf16_f32 v83, v88, v89
	v_pk_mul_f32 v[152:153], v[140:141], v[122:123] op_sel_hi:[0,1]
	v_cvt_pk_bf16_f32 v84, v84, v85
	v_cvt_pk_bf16_f32 v85, v118, v119
	global_store_dwordx4 v[144:145], v[82:85], off offset:256
	v_pk_mul_f32 v[154:155], v[140:141], v[124:125] op_sel_hi:[0,1]
	v_pk_mul_f32 v[150:151], v[140:141], v[128:129] op_sel_hi:[0,1]
	v_lshlrev_b64 v[82:83], 14, v[90:91]
	v_lshl_add_u64 v[82:83], s[0:1], 0, v[82:83]
	v_lshl_add_u64 v[96:97], v[82:83], 0, v[148:149]
	global_load_dwordx4 v[82:85], v[96:97], off nt
	global_load_dwordx4 v[86:89], v[96:97], off offset:16 nt
	global_load_dwordx4 v[118:121], v[96:97], off offset:528 nt
	global_load_dwordx4 v[142:145], v[96:97], off offset:512 nt
	v_pk_mul_f32 v[96:97], v[140:141], v[126:127] op_sel_hi:[0,1]
	v_cvt_f32_i32_e32 v41, v41
	v_cvt_f32_i32_e32 v40, v40
	v_cvt_f32_i32_e32 v35, v35
	v_cvt_f32_i32_e32 v34, v34
	v_cvt_f32_i32_e32 v31, v31
	v_cvt_f32_i32_e32 v30, v30
	v_cvt_f32_i32_e32 v27, v27
	s_waitcnt vmcnt(9)
	v_pk_fma_f32 v[78:79], v[96:97], v[78:79], v[98:99]
	s_waitcnt vmcnt(8)
;     __device__ __forceinline__ void operator()(const f32x4 (&acc)[2][2][4][2], const Unit& u, int wr, int wc, int fr, int fq) const {
;     ...
;         EPB_LOAD(0);
; #pragma unroll
;         for (int kb = 0; kb < 8; ++kb) { const int ai = kb >> 2, m = kb & 3;
;             if (kb < 7) EPB_LOAD(kb + 1);
;             { const int row = row0 + ai * HALF + m * 16; float rmx = 0.f;
; #pragma unroll
;                 for (int bj = 0; bj < 2; ++bj) { const int col = col0 + bj * HALF; f32x4 v0 = acc[ai][bj][m][0], v1 = acc[ai][bj][m][1];
;                     if (QI8) { const f32x4 c0 = cb[bj][0] * ra[ai][m], c1 = cb[bj][1] * ra[ai][m]; const i32x4 i0 = __builtin_bit_cast(i32x4, v0), i1 = __builtin_bit_cast(i32x4, v1);
;                         v0 = (f32x4){(float)i0[0], (float)i0[1], (float)i0[2], (float)i0[3]} * c0; v1 = (f32x4){(float)i1[0], (float)i1[1], (float)i1[2], (float)i1[3]} * c1; }
;                     else if (MODE == 0) { v0 = v0 * tsc; v1 = v1 * tsc; }
;                     if (!QI8 && MODE == 1) { v0 = v0 * cb[bj][0]; v1 = v1 * cb[bj][1]; }
;                     if (MODE == 2 || MODE == 3) { const u32x4 g = gq[kb & 1][bj];
;                         f32x4 g0 = {sigmoidf_(bflo(g.x)), sigmoidf_(bfhi(g.x)), sigmoidf_(bflo(g.y)), sigmoidf_(bfhi(g.y))};
;                         f32x4 g1 = {sigmoidf_(bflo(g.z)), sigmoidf_(bfhi(g.z)), sigmoidf_(bflo(g.w)), sigmoidf_(bfhi(g.w))};
;                         v0 = v0 * g0; v1 = v1 * g1;
;                         if (MODE == 3) { const u32x4 q = aq[kb & 1][bj];
;                             v0 = v0 + (f32x4){bflo(q.x), bfhi(q.x), bflo(q.y), bfhi(q.y)}; v1 = v1 + (f32x4){bflo(q.z), bfhi(q.z), bflo(q.w), bfhi(q.w)}; } }
;                     if (MODE == 4) { v0 = v0 + rs[kb & 1][bj][0]; v1 = v1 + rs[kb & 1][bj][1]; }
;                     if (MODE == 5) { const u32x4 c = gq[kb & 1][bj], q = aq[kb & 1][bj];
;                         v0 = (f32x4){bflo(c.x) + sigmoidf_(v0[0]) * bflo(q.x), bfhi(c.x) + sigmoidf_(v0[1]) * bfhi(q.x), bflo(c.y) + sigmoidf_(v0[2]) * bflo(q.y), bfhi(c.y) + sigmoidf_(v0[3]) * bfhi(q.y)};
;                         v1 = (f32x4){bflo(c.z) + sigmoidf_(v1[0]) * bflo(q.z), bfhi(c.z) + sigmoidf_(v1[1]) * bfhi(q.z), bflo(c.w) + sigmoidf_(v1[2]) * bflo(q.w), bfhi(c.w) + sigmoidf_(v1[3]) * bfhi(q.w)}; }
	v_pk_fma_f32 v[96:97], v[154:155], v[76:77], v[104:105]
	v_pk_fma_f32 v[76:77], v[152:153], v[74:75], v[102:103]
	v_cvt_pk_bf16_f32 v74, v78, v79
	v_lshlrev_b64 v[78:79], 13, v[166:167]
	v_lshl_add_u64 v[78:79], s[10:11], 0, v[78:79]
	v_pk_fma_f32 v[80:81], v[150:151], v[80:81], v[100:101]
	v_lshl_add_u64 v[78:79], v[78:79], 0, v[130:131]
	v_cvt_pk_bf16_f32 v75, v80, v81
	v_cvt_pk_bf16_f32 v76, v76, v77
	v_cvt_pk_bf16_f32 v77, v96, v97
	global_store_dwordx4 v[78:79], v[74:77], off
	v_pk_mul_f32 v[80:81], v[140:141], v[106:107] op_sel_hi:[0,1]
	v_pk_mul_f32 v[96:97], v[140:141], v[108:109] op_sel_hi:[0,1]
	v_pk_mul_f32 v[74:75], v[140:141], v[110:111] op_sel_hi:[0,1]
	v_pk_mul_f32 v[76:77], v[140:141], v[112:113] op_sel_hi:[0,1]
	s_waitcnt vmcnt(7)
	v_pk_fma_f32 v[70:71], v[74:75], v[70:71], v[114:115]
	v_pk_fma_f32 v[74:75], v[96:97], v[68:69], v[94:95]
	v_pk_fma_f32 v[68:69], v[80:81], v[66:67], v[92:93]
	v_add_u32_e32 v92, 0x90, v146
	v_pk_fma_f32 v[72:73], v[76:77], v[72:73], v[116:117]
	v_cvt_pk_bf16_f32 v66, v70, v71
	v_ashrrev_i32_e32 v93, 31, v92
	v_cvt_pk_bf16_f32 v67, v72, v73
	v_cvt_pk_bf16_f32 v68, v68, v69
	v_cvt_pk_bf16_f32 v69, v74, v75
	global_store_dwordx4 v[78:79], v[66:69], off offset:256
	v_pk_mul_f32 v[94:95], v[138:139], v[126:127] op_sel_hi:[0,1]
	v_pk_mul_f32 v[98:99], v[138:139], v[122:123] op_sel_hi:[0,1]
	v_lshlrev_b64 v[66:67], 14, v[92:93]
	v_lshl_add_u64 v[66:67], s[0:1], 0, v[66:67]
	v_lshl_add_u64 v[78:79], v[66:67], 0, v[148:149]
	global_load_dwordx4 v[66:69], v[78:79], off nt
	global_load_dwordx4 v[70:73], v[78:79], off offset:16 nt
	global_load_dwordx4 v[74:77], v[78:79], off offset:528 nt
	s_nop 0
	global_load_dwordx4 v[78:81], v[78:79], off offset:512 nt
	v_pk_mul_f32 v[100:101], v[138:139], v[124:125] op_sel_hi:[0,1]
	v_pk_mul_f32 v[96:97], v[138:139], v[128:129] op_sel_hi:[0,1]
	v_cvt_f32_i32_e32 v29, v29
	v_cvt_f32_i32_e32 v28, v28
	v_cvt_f32_i32_e32 v26, v26
	v_cvt_f32_i32_e32 v33, v33
	v_cvt_f32_i32_e32 v32, v32
	v_cvt_f32_i32_e32 v23, v23
	v_cvt_f32_i32_e32 v22, v22
	v_cvt_f32_i32_e32 v25, v25
	v_cvt_f32_i32_e32 v24, v24
	v_cvt_f32_i32_e32 v19, v19
	v_cvt_f32_i32_e32 v21, v21
	v_cvt_f32_i32_e32 v20, v20
	v_cvt_f32_i32_e32 v18, v18
	v_cvt_f32_i32_e32 v15, v15
	v_cvt_f32_i32_e32 v14, v14
	v_cvt_f32_i32_e32 v11, v11
	v_cvt_f32_i32_e32 v13, v13
	v_cvt_f32_i32_e32 v12, v12
	v_cvt_f32_i32_e32 v10, v10
	v_cvt_f32_i32_e32 v17, v17
	v_cvt_f32_i32_e32 v16, v16
	v_cvt_f32_i32_e32 v7, v7
	v_cvt_f32_i32_e32 v6, v6
	v_cvt_f32_i32_e32 v3, v3
	v_cvt_f32_i32_e32 v5, v5
	v_cvt_f32_i32_e32 v4, v4
	v_cvt_f32_i32_e32 v2, v2
	v_cvt_f32_i32_e32 v9, v9
	v_cvt_f32_i32_e32 v8, v8
	s_andn2_b64 vcc, exec, s[6:7]
	s_mov_b64 s[6:7], -1
	s_waitcnt vmcnt(9)
	v_pk_fma_f32 v[62:63], v[94:95], v[62:63], v[82:83]
	s_waitcnt vmcnt(8)
	v_pk_fma_f32 v[82:83], v[100:101], v[60:61], v[88:89]
	v_pk_fma_f32 v[60:61], v[98:99], v[58:59], v[86:87]
	v_cvt_pk_bf16_f32 v58, v62, v63
	v_lshlrev_b64 v[62:63], 13, v[90:91]
	v_lshl_add_u64 v[62:63], s[10:11], 0, v[62:63]
	v_pk_fma_f32 v[64:65], v[96:97], v[64:65], v[84:85]
	v_lshl_add_u64 v[62:63], v[62:63], 0, v[130:131]
	v_cvt_pk_bf16_f32 v59, v64, v65
	v_cvt_pk_bf16_f32 v60, v60, v61
	v_cvt_pk_bf16_f32 v61, v82, v83
	global_store_dwordx4 v[62:63], v[58:61], off
	v_pk_mul_f32 v[82:83], v[138:139], v[108:109] op_sel_hi:[0,1]
	v_pk_mul_f32 v[64:65], v[138:139], v[106:107] op_sel_hi:[0,1]
	v_pk_mul_f32 v[58:59], v[138:139], v[110:111] op_sel_hi:[0,1]
	v_pk_mul_f32 v[60:61], v[138:139], v[112:113] op_sel_hi:[0,1]
	s_waitcnt vmcnt(7)
	v_pk_fma_f32 v[54:55], v[58:59], v[54:55], v[142:143]
	v_pk_fma_f32 v[58:59], v[82:83], v[52:53], v[120:121]
	v_add_u32_e32 v82, 0xa0, v146
	v_pk_fma_f32 v[56:57], v[60:61], v[56:57], v[144:145]
	v_pk_fma_f32 v[52:53], v[64:65], v[50:51], v[118:119]
	v_cvt_pk_bf16_f32 v50, v54, v55
	v_cvt_pk_bf16_f32 v51, v56, v57
	v_ashrrev_i32_e32 v83, 31, v82
	v_cvt_pk_bf16_f32 v52, v52, v53
	v_cvt_pk_bf16_f32 v53, v58, v59
	global_store_dwordx4 v[62:63], v[50:53], off offset:256
	v_pk_mul_f32 v[84:85], v[136:137], v[126:127] op_sel_hi:[0,1]
	v_pk_mul_f32 v[88:89], v[136:137], v[122:123] op_sel_hi:[0,1]
	v_lshlrev_b64 v[50:51], 14, v[82:83]
	v_lshl_add_u64 v[50:51], s[0:1], 0, v[50:51]
	v_lshl_add_u64 v[62:63], v[50:51], 0, v[148:149]
	v_pk_mul_f32 v[90:91], v[136:137], v[124:125] op_sel_hi:[0,1]
	global_load_dwordx4 v[50:53], v[62:63], off offset:16 nt
	global_load_dwordx4 v[54:57], v[62:63], off nt
	global_load_dwordx4 v[58:61], v[62:63], off offset:528 nt
	s_nop 0
	global_load_dwordx4 v[62:65], v[62:63], off offset:512 nt
	v_pk_mul_f32 v[86:87], v[136:137], v[128:129] op_sel_hi:[0,1]
	s_waitcnt vmcnt(9)
	v_pk_fma_f32 v[46:47], v[84:85], v[46:47], v[66:67]
	s_waitcnt vmcnt(8)
;     __device__ __forceinline__ void operator()(const f32x4 (&acc)[2][2][4][2], const Unit& u, int wr, int wc, int fr, int fq) const {
;     ...
;         for (int kb = 0; kb < 8; ++kb) { const int ai = kb >> 2, m = kb & 3;
;             if (kb < 7) EPB_LOAD(kb + 1);
;             { const int row = row0 + ai * HALF + m * 16; float rmx = 0.f;
; #pragma unroll
;                 for (int bj = 0; bj < 2; ++bj) { const int col = col0 + bj * HALF; f32x4 v0 = acc[ai][bj][m][0], v1 = acc[ai][bj][m][1];
;                     if (QI8) { const f32x4 c0 = cb[bj][0] * ra[ai][m], c1 = cb[bj][1] * ra[ai][m]; const i32x4 i0 = __builtin_bit_cast(i32x4, v0), i1 = __builtin_bit_cast(i32x4, v1);
;                         v0 = (f32x4){(float)i0[0], (float)i0[1], (float)i0[2], (float)i0[3]} * c0; v1 = (f32x4){(float)i1[0], (float)i1[1], (float)i1[2], (float)i1[3]} * c1; }
;                     else if (MODE == 0) { v0 = v0 * tsc; v1 = v1 * tsc; }
;                     if (!QI8 && MODE == 1) { v0 = v0 * cb[bj][0]; v1 = v1 * cb[bj][1]; }
;                     if (MODE == 2 || MODE == 3) { const u32x4 g = gq[kb & 1][bj];
;                         f32x4 g0 = {sigmoidf_(bflo(g.x)), sigmoidf_(bfhi(g.x)), sigmoidf_(bflo(g.y)), sigmoidf_(bfhi(g.y))};
;                         f32x4 g1 = {sigmoidf_(bflo(g.z)), sigmoidf_(bfhi(g.z)), sigmoidf_(bflo(g.w)), sigmoidf_(bfhi(g.w))};
;                         v0 = v0 * g0; v1 = v1 * g1;
;                         if (MODE == 3) { const u32x4 q = aq[kb & 1][bj];
;                             v0 = v0 + (f32x4){bflo(q.x), bfhi(q.x), bflo(q.y), bfhi(q.y)}; v1 = v1 + (f32x4){bflo(q.z), bfhi(q.z), bflo(q.w), bfhi(q.w)}; } }
;                     if (MODE == 4) { v0 = v0 + rs[kb & 1][bj][0]; v1 = v1 + rs[kb & 1][bj][1]; }
;                     if (MODE == 5) { const u32x4 c = gq[kb & 1][bj], q = aq[kb & 1][bj];
;                         v0 = (f32x4){bflo(c.x) + sigmoidf_(v0[0]) * bflo(q.x), bfhi(c.x) + sigmoidf_(v0[1]) * bfhi(q.x), bflo(c.y) + sigmoidf_(v0[2]) * bflo(q.y), bfhi(c.y) + sigmoidf_(v0[3]) * bfhi(q.y)};
;                         v1 = (f32x4){bflo(c.z) + sigmoidf_(v1[0]) * bflo(q.z), bfhi(c.z) + sigmoidf_(v1[1]) * bfhi(q.z), bflo(c.w) + sigmoidf_(v1[2]) * bflo(q.w), bfhi(c.w) + sigmoidf_(v1[3]) * bfhi(q.w)}; }
;                     u32x4 w; w.x = cvtpk(v0[0], v0[1]); w.y = cvtpk(v0[2], v0[3]); w.z = cvtpk(v1[0], v1[1]); w.w = cvtpk(v1[2], v1[3]);
	v_pk_fma_f32 v[66:67], v[90:91], v[44:45], v[72:73]
	v_pk_fma_f32 v[44:45], v[88:89], v[42:43], v[70:71]
	v_cvt_pk_bf16_f32 v42, v46, v47
	v_lshlrev_b64 v[46:47], 13, v[92:93]
	v_lshl_add_u64 v[46:47], s[10:11], 0, v[46:47]
	v_pk_fma_f32 v[48:49], v[86:87], v[48:49], v[68:69]
	v_lshl_add_u64 v[46:47], v[46:47], 0, v[130:131]
	v_cvt_pk_bf16_f32 v43, v48, v49
	v_cvt_pk_bf16_f32 v44, v44, v45
	v_cvt_pk_bf16_f32 v45, v66, v67
	global_store_dwordx4 v[46:47], v[42:45], off
	v_pk_mul_f32 v[66:67], v[136:137], v[108:109] op_sel_hi:[0,1]
	v_pk_mul_f32 v[48:49], v[136:137], v[106:107] op_sel_hi:[0,1]
	v_pk_mul_f32 v[42:43], v[136:137], v[110:111] op_sel_hi:[0,1]
	v_pk_mul_f32 v[44:45], v[136:137], v[112:113] op_sel_hi:[0,1]
	s_waitcnt vmcnt(7)
	v_pk_fma_f32 v[38:39], v[42:43], v[38:39], v[78:79]
	v_pk_fma_f32 v[42:43], v[66:67], v[36:37], v[76:77]
	v_add_u32_e32 v66, 0xb0, v146
	v_pk_fma_f32 v[40:41], v[44:45], v[40:41], v[80:81]
	v_pk_fma_f32 v[36:37], v[48:49], v[34:35], v[74:75]
	v_cvt_pk_bf16_f32 v34, v38, v39
	v_cvt_pk_bf16_f32 v35, v40, v41
	v_ashrrev_i32_e32 v67, 31, v66
	v_cvt_pk_bf16_f32 v36, v36, v37
	v_cvt_pk_bf16_f32 v37, v42, v43
	global_store_dwordx4 v[46:47], v[34:37], off offset:256
	v_pk_mul_f32 v[68:69], v[134:135], v[126:127] op_sel_hi:[0,1]
	v_pk_mul_f32 v[72:73], v[134:135], v[122:123] op_sel_hi:[0,1]
	v_lshlrev_b64 v[34:35], 14, v[66:67]
	v_lshl_add_u64 v[34:35], s[0:1], 0, v[34:35]
	v_lshl_add_u64 v[46:47], v[34:35], 0, v[148:149]
	global_load_dwordx4 v[34:37], v[46:47], off nt
	global_load_dwordx4 v[38:41], v[46:47], off offset:16 nt
	global_load_dwordx4 v[42:45], v[46:47], off offset:528 nt
	s_nop 0
	global_load_dwordx4 v[46:49], v[46:47], off offset:512 nt
	v_pk_mul_f32 v[74:75], v[134:135], v[124:125] op_sel_hi:[0,1]
	v_pk_mul_f32 v[70:71], v[134:135], v[128:129] op_sel_hi:[0,1]
	s_waitcnt vmcnt(9)
	v_pk_fma_f32 v[52:53], v[74:75], v[28:29], v[52:53]
	s_waitcnt vmcnt(8)
	v_pk_fma_f32 v[30:31], v[68:69], v[30:31], v[54:55]
	v_pk_fma_f32 v[28:29], v[72:73], v[26:27], v[50:51]
	v_cvt_pk_bf16_f32 v26, v30, v31
	v_lshlrev_b64 v[30:31], 13, v[82:83]
	v_lshl_add_u64 v[30:31], s[10:11], 0, v[30:31]
	v_pk_fma_f32 v[32:33], v[70:71], v[32:33], v[56:57]
	v_lshl_add_u64 v[30:31], v[30:31], 0, v[130:131]
	v_cvt_pk_bf16_f32 v27, v32, v33
	v_cvt_pk_bf16_f32 v28, v28, v29
	v_cvt_pk_bf16_f32 v29, v52, v53
	global_store_dwordx4 v[30:31], v[26:29], off
	v_pk_mul_f32 v[32:33], v[134:135], v[106:107] op_sel_hi:[0,1]
	v_pk_mul_f32 v[50:51], v[134:135], v[108:109] op_sel_hi:[0,1]
	v_pk_mul_f32 v[26:27], v[134:135], v[110:111] op_sel_hi:[0,1]
	v_pk_mul_f32 v[28:29], v[134:135], v[112:113] op_sel_hi:[0,1]
	s_waitcnt vmcnt(7)
	v_pk_fma_f32 v[24:25], v[28:29], v[24:25], v[64:65]
	v_pk_fma_f32 v[22:23], v[26:27], v[22:23], v[62:63]
	v_pk_fma_f32 v[26:27], v[50:51], v[20:21], v[60:61]
	v_pk_fma_f32 v[20:21], v[32:33], v[18:19], v[58:59]
	v_cvt_pk_bf16_f32 v18, v22, v23
	v_cvt_pk_bf16_f32 v19, v24, v25
	v_pk_mul_f32 v[22:23], v[132:133], v[122:123] op_sel_hi:[0,1]
	v_cvt_pk_bf16_f32 v20, v20, v21
	v_cvt_pk_bf16_f32 v21, v26, v27
	global_store_dwordx4 v[30:31], v[18:21], off offset:256
	v_pk_mul_f32 v[24:25], v[132:133], v[124:125] op_sel_hi:[0,1]
	s_nop 0
	v_pk_mul_f32 v[18:19], v[126:127], v[132:133] op_sel_hi:[1,0]
	v_pk_mul_f32 v[20:21], v[128:129], v[132:133] op_sel_hi:[1,0]
	s_waitcnt vmcnt(5)
	v_pk_fma_f32 v[14:15], v[18:19], v[14:15], v[34:35]
	s_waitcnt vmcnt(4)
	v_pk_fma_f32 v[18:19], v[24:25], v[12:13], v[40:41]
	v_pk_fma_f32 v[12:13], v[22:23], v[10:11], v[38:39]
	v_cvt_pk_bf16_f32 v10, v14, v15
	v_lshlrev_b64 v[14:15], 13, v[66:67]
	v_lshl_add_u64 v[14:15], s[10:11], 0, v[14:15]
	v_pk_fma_f32 v[16:17], v[20:21], v[16:17], v[36:37]
	v_lshl_add_u64 v[14:15], v[14:15], 0, v[130:131]
	v_cvt_pk_bf16_f32 v11, v16, v17
	v_cvt_pk_bf16_f32 v12, v12, v13
	v_cvt_pk_bf16_f32 v13, v18, v19
	global_store_dwordx4 v[14:15], v[10:13], off
	v_pk_mul_f32 v[16:17], v[132:133], v[106:107] op_sel_hi:[0,1]
	v_pk_mul_f32 v[18:19], v[132:133], v[108:109] op_sel_hi:[0,1]
	v_pk_mul_f32 v[10:11], v[132:133], v[110:111] op_sel_hi:[0,1]
	v_pk_mul_f32 v[12:13], v[132:133], v[112:113] op_sel_hi:[0,1]
	s_waitcnt vmcnt(3)
	v_pk_fma_f32 v[6:7], v[10:11], v[6:7], v[46:47]
	v_pk_fma_f32 v[10:11], v[18:19], v[4:5], v[44:45]
	v_pk_fma_f32 v[4:5], v[16:17], v[2:3], v[42:43]
	v_pk_fma_f32 v[8:9], v[12:13], v[8:9], v[48:49]
	v_cvt_pk_bf16_f32 v2, v6, v7
	s_nop 0
	v_cvt_pk_bf16_f32 v3, v8, v9
	v_cvt_pk_bf16_f32 v4, v4, v5
	v_cvt_pk_bf16_f32 v5, v10, v11
	global_store_dwordx4 v[14:15], v[2:5], off offset:256
	s_cbranch_vccnz .LBB0_1173
	s_andn2_b64 vcc, exec, s[2:3]
	s_cbranch_vccnz .LBB0_1172
	s_barrier
	s_branch .LBB0_1172
